# on top of the XCD-contiguous MoE order: waves 4-7 of every workgroup enter the lockstep element-wise phases 2, 6 and 15 half an iteration late (s_sleep) so one half computes under the other half's mem
# speedup vs baseline: 1.0129x; 1.0129x over previous
.LBB0_193:
	s_or_b64 exec, exec, s[18:19]
	v_mov_b32_e32 v2, v0
	s_waitcnt lgkmcnt(0)
	s_barrier
	v_readfirstlane_b32 s96, v0
	s_nop 3
	s_bitcmp1_b32 s96, 8
	s_cbranch_scc0 .Lskew_P2
	s_sleep 127
	s_sleep 53

.LBB0_551:
	s_or_b64 exec, exec, s[18:19]
	v_mov_b32_e32 v36, v0
	s_waitcnt lgkmcnt(0)
	s_barrier
	v_readfirstlane_b32 s96, v0
	s_nop 3
	s_bitcmp1_b32 s96, 8
	s_cbranch_scc0 .Lskew_P6
	s_sleep 127
	s_sleep 127
	s_sleep 36
.Lskew_P6:
	s_mov_b32 s23, s93
	v_readfirstlane_b32 s4, v36
	s_ashr_i32 s22, s4, 6
	v_readlane_b32 s4, v253, 62
	s_add_i32 s34, s22, s4
	s_mov_b64 s[4:5], s[62:63]
	s_mov_b32 s20, 13
	s_mov_b32 s14, 14
	s_cmpk_gt_i32 s34, 0x1fff
	s_cbranch_scc1 .LBB0_554
	s_lshl_b32 s35, s23, 3
	s_add_u32 s18, s4, 0xc800000
	s_addc_u32 s19, s5, 0
	s_ashr_i32 s21, s20, 31
	s_lshl_b64 s[16:17], s[20:21], 3
	s_add_u32 s16, s84, s16
	s_addc_u32 s17, s85, s17
	s_add_u32 s36, s4, 0x4f500000
	s_addc_u32 s37, s5, 0
	s_ashr_i32 s15, s14, 31
	s_lshl_b64 s[14:15], s[14:15], 3
	s_add_u32 s14, s84, s14
	s_addc_u32 s15, s85, s15
	s_load_dwordx2 s[14:15], s[14:15], 0x0
	v_readlane_b32 s6, v252, 37
	s_load_dwordx2 s[16:17], s[16:17], 0x0
	v_readlane_b32 s7, v252, 38
	s_lshl_b64 s[20:21], s[6:7], 2
	s_waitcnt lgkmcnt(0)
	s_add_u32 s14, s14, s20
	s_addc_u32 s15, s15, s21
	v_and_b32_e32 v34, 63, v36
	s_add_u32 s16, s16, s20
	v_lshlrev_b32_e32 v1, 5, v34
	s_addc_u32 s17, s17, s21
	global_load_dwordx4 v[2:5], v1, s[14:15] offset:2048
	global_load_dwordx4 v[6:9], v1, s[14:15] offset:2064
	global_load_dwordx4 v[10:13], v1, s[16:17] offset:2048
	global_load_dwordx4 v[14:17], v1, s[16:17] offset:2064
	global_load_dwordx4 v[18:21], v1, s[14:15]
	global_load_dwordx4 v[22:25], v1, s[14:15] offset:16
	global_load_dwordx4 v[26:29], v1, s[16:17]
	global_load_dwordx4 v[30:33], v1, s[16:17] offset:16
	s_add_u32 s16, s4, 0x1a800000
	s_addc_u32 s17, s5, 0
	s_add_u32 s20, s4, 0x30800000
	s_addc_u32 s21, s5, 0
	s_add_u32 s4, s4, 0x1e800000
	v_lshlrev_b32_e32 v34, 4, v34
	s_addc_u32 s5, s5, 0
	v_and_b32_e32 v140, 0x70, v34
	v_lshl_add_u64 v[142:143], s[4:5], 0, v[34:35]
	v_or_b32_e32 v34, 0x400, v34
	v_lshlrev_b32_e32 v1, 6, v36
	v_lshl_add_u64 v[144:145], s[4:5], 0, v[34:35]
	s_lshl_b32 s4, s22, 2
	v_readlane_b32 s5, v252, 15
	v_and_b32_e32 v1, 0x1c0, v1
	v_bfe_u32 v141, v36, 3, 3
	s_add_i32 s22, s5, s4
	s_lshl_b32 s4, s23, 5

.LBB0_1267:
	v_readfirstlane_b32 s96, v0
	s_nop 3
	s_bitcmp1_b32 s96, 8
	s_cbranch_scc0 .Lskew_P15
	s_sleep 127
	s_sleep 73
